# batch 3 plus non-temporal stores for the attention output rows
# baseline (speedup 1.0000x reference)
; DI unsigned pk4_fp8(float a, float b, float c, float d) { int r = 0; r = __builtin_amdgcn_cvt_pk_fp8_f32(sat8(a), sat8(b), r, false); r = __builtin_amdgcn_cvt_pk_fp8_f32(sat8(c), sat8(d), r, true); return (unsigned)r; }
; DI float half_sum(float v) { const auto rr = __builtin_amdgcn_permlane32_swap(__float_as_uint(v), __float_as_uint(v), false, false); return __uint_as_float(rr[0]) + __uint_as_float(rr[1]); }
; DI void phase_attn(Frame& F, int l) {
;     ...
;         const float ltot = half_sum(l_run); const float inv = AZ8_SCALE / ltot;
; #pragma unroll
;         for (int ds = 0; ds < 2; ++ds)
; #pragma unroll
;             for (int g4 = 0; g4 < 4; g4 += 2) {
;                 const unsigned wa = pk4_fp8(o[ds][4 * g4] * inv, o[ds][4 * g4 + 1] * inv, o[ds][4 * g4 + 2] * inv, o[ds][4 * g4 + 3] * inv), wb = pk4_fp8(o[ds][4 * g4 + 4] * inv, o[ds][4 * g4 + 5] * inv, o[ds][4 * g4 + 6] * inv, o[ds][4 * g4 + 7] * inv);
;                 const auto rr = __builtin_amdgcn_permlane32_swap(wa, wb, false, false);
;                 u32x2 w; w.x = rr[0]; w.y = rr[1];
;                 *(u32x2*)(att + qtok * D + h * HD + 32 * ds + 8 * (g4 + hh)) = w; }
;         if (!((F.bid & 1) && it == 3)) { __syncthreads(); run_items1(F, 1 + l, SLOT_ITEMS, cq); }
.LBB0_568:
	v_mov_b32_e32 v0, v11
	s_nop 1
	v_permlane32_swap_b32_e32 v11, v0
	v_add_f32_e32 v0, v11, v0
	s_mov_b32 s2, 0x41000000
	s_waitcnt vmcnt(1)
	v_div_scale_f32 v2, s[0:1], v0, v0, s2
	v_rcp_f32_e32 v3, v2
	v_readlane_b32 s0, v253, 21
	v_readlane_b32 s1, v253, 22
	s_bitcmp1_b32 s19, 0
	v_fma_f32 v4, -v2, v3, 1.0
	v_fmac_f32_e32 v3, v4, v3
	v_div_scale_f32 v4, vcc, s2, v0, s2
	v_mul_f32_e32 v5, v4, v3
	s_waitcnt vmcnt(0)
	v_fma_f32 v6, -v2, v5, v4
	v_fmac_f32_e32 v5, v6, v3
	v_fma_f32 v2, -v2, v5, v4
	v_div_fmas_f32 v2, v2, v3, v5
	v_div_fixup_f32 v0, v2, v0, s2
	v_mul_f32_e32 v2, v16, v0
	v_mul_f32_e32 v3, v17, v0
	v_med3_f32 v5, v2, s53, v204
	v_med3_f32 v3, v3, s53, v204
	v_mov_b32_e32 v2, v1
	v_cvt_pk_fp8_f32 v2, v5, v3
	v_mul_f32_e32 v4, v18, v0
	v_mul_f32_e32 v3, v19, v0
	v_med3_f32 v4, v4, s53, v204
	v_med3_f32 v3, v3, s53, v204
	v_cvt_pk_fp8_f32 v2, v4, v3 op_sel:[0,0,1]
	v_mul_f32_e32 v3, v20, v0
	v_mul_f32_e32 v4, v21, v0
	v_med3_f32 v6, v3, s53, v204
	v_med3_f32 v4, v4, s53, v204
	v_mov_b32_e32 v3, v1
	v_cvt_pk_fp8_f32 v3, v6, v4
	v_mul_f32_e32 v6, v24, v0
	v_mul_f32_e32 v7, v25, v0
	v_med3_f32 v9, v6, s53, v204
	v_med3_f32 v7, v7, s53, v204
	v_mov_b32_e32 v6, v1
	v_cvt_pk_fp8_f32 v6, v9, v7
	v_mul_f32_e32 v8, v26, v0
	v_mul_f32_e32 v7, v27, v0
	v_med3_f32 v8, v8, s53, v204
	v_med3_f32 v7, v7, s53, v204
	v_cvt_pk_fp8_f32 v6, v8, v7 op_sel:[0,0,1]
	v_mul_f32_e32 v7, v28, v0
	v_mul_f32_e32 v8, v29, v0
	v_med3_f32 v10, v7, s53, v204
	v_med3_f32 v8, v8, s53, v204
	v_mov_b32_e32 v7, v1
	v_cvt_pk_fp8_f32 v7, v10, v8
	v_mul_f32_e32 v5, v22, v0
	v_mul_f32_e32 v4, v23, v0
	v_med3_f32 v5, v5, s53, v204
	v_med3_f32 v4, v4, s53, v204
	v_mul_f32_e32 v9, v30, v0
	v_mul_f32_e32 v8, v31, v0
	v_cvt_pk_fp8_f32 v3, v5, v4 op_sel:[0,0,1]
	v_med3_f32 v9, v9, s53, v204
	v_med3_f32 v8, v8, s53, v204
	v_cvt_pk_fp8_f32 v7, v9, v8 op_sel:[0,0,1]
	v_lshl_add_u64 v[4:5], s[0:1], 0, v[170:171]
	v_lshl_add_u64 v[4:5], v[4:5], 0, s[58:59]
	v_permlane32_swap_b32_e32 v2, v3
	v_lshl_add_u64 v[4:5], v[4:5], 0, v[168:169]
	global_store_dwordx2 v[4:5], v[2:3], off nt
	v_permlane32_swap_b32_e32 v6, v7
	v_mul_f32_e32 v2, v32, v0
	v_mul_f32_e32 v3, v33, v0
	global_store_dwordx2 v[4:5], v[6:7], off offset:16 nt
	v_med3_f32 v7, v2, s53, v204
	v_med3_f32 v3, v3, s53, v204
	v_mov_b32_e32 v2, v1
	v_cvt_pk_fp8_f32 v2, v7, v3
	v_mul_f32_e32 v6, v34, v0
	v_mul_f32_e32 v3, v35, v0
	v_med3_f32 v6, v6, s53, v204
	v_med3_f32 v3, v3, s53, v204
	v_cvt_pk_fp8_f32 v2, v6, v3 op_sel:[0,0,1]
	v_mul_f32_e32 v3, v36, v0
	v_mul_f32_e32 v6, v37, v0
	v_med3_f32 v8, v3, s53, v204
	v_med3_f32 v6, v6, s53, v204
	v_mov_b32_e32 v3, v1
	v_cvt_pk_fp8_f32 v3, v8, v6
	v_mul_f32_e32 v7, v38, v0
	v_mul_f32_e32 v6, v39, v0
	v_med3_f32 v7, v7, s53, v204
	v_med3_f32 v6, v6, s53, v204
	v_cvt_pk_fp8_f32 v3, v7, v6 op_sel:[0,0,1]
	v_mul_f32_e32 v6, v40, v0
	v_mul_f32_e32 v7, v41, v0
	v_med3_f32 v9, v6, s53, v204
	v_med3_f32 v7, v7, s53, v204
	v_mov_b32_e32 v6, v1
	v_cvt_pk_fp8_f32 v6, v9, v7
	v_mul_f32_e32 v8, v42, v0
	v_mul_f32_e32 v7, v43, v0
	v_med3_f32 v8, v8, s53, v204
	v_med3_f32 v7, v7, s53, v204
	v_cvt_pk_fp8_f32 v6, v8, v7 op_sel:[0,0,1]
	v_mul_f32_e32 v7, v44, v0
	v_mul_f32_e32 v8, v45, v0
	v_med3_f32 v10, v7, s53, v204
	v_med3_f32 v8, v8, s53, v204
	v_mov_b32_e32 v7, v1
	v_cvt_pk_fp8_f32 v7, v10, v8
	v_mul_f32_e32 v9, v46, v0
	v_mul_f32_e32 v0, v47, v0
	v_med3_f32 v8, v9, s53, v204
	v_med3_f32 v0, v0, s53, v204
	v_cvt_pk_fp8_f32 v7, v8, v0 op_sel:[0,0,1]
	s_cselect_b64 s[0:1], -1, 0
	s_cmp_eq_u32 s18, 3
	s_cselect_b64 s[2:3], -1, 0
	s_and_b64 s[0:1], s[2:3], s[0:1]
	v_permlane32_swap_b32_e32 v2, v3
	v_permlane32_swap_b32_e32 v6, v7
	s_and_b64 vcc, exec, s[0:1]
	global_store_dwordx2 v[4:5], v[2:3], off offset:32 nt
	global_store_dwordx2 v[4:5], v[6:7], off offset:48 nt
	s_cbranch_vccnz .LBB0_474
	s_mov_b64 s[6:7], s[70:71]
	s_cmp_lg_u32 s63, 8
	s_barrier
	s_cbranch_scc1 .LBB0_575
	v_mov_b32_e32 v0, 0
	s_and_saveexec_b64 s[2:3], s[4:5]
	s_cbranch_execz .LBB0_574
	s_mov_b64 s[10:11], exec
	v_mbcnt_lo_u32_b32 v0, s10, 0
	v_mbcnt_hi_u32_b32 v0, s11, v0
	v_cmp_eq_u32_e32 vcc, 0, v0
	s_and_saveexec_b64 s[8:9], vcc
	s_cbranch_execz .LBB0_573
	s_bcnt1_i32_b64 s0, s[10:11]
	s_lshl_b32 s0, s0, 3
	v_mov_b32_e32 v2, s0
	global_atomic_add v2, v1, v2, s[12:13] sc0
